# rowpass adaLN/post-norm vector staging rewritten: all ten loads in flight before one wait (was one L2 round trip per pair)
# speedup vs baseline: 1.0291x; 1.0087x over previous
.LBB0_271:
	s_lshl_b32 s16, s50, 6
	s_add_i32 s14, s16, s37
	s_ashr_i32 s15, s14, 31
	s_lshl_b64 s[20:21], s[14:15], 12
	s_waitcnt vmcnt(0)
	v_lshl_add_u64 v[12:13], v[38:39], 0, s[20:21]
	global_load_dwordx4 v[0:3], v[12:13], off
	global_load_dwordx4 v[4:7], v[12:13], off offset:1024
	global_load_dwordx4 v[8:11], v[12:13], off offset:2048
	s_nop 0
	global_load_dwordx4 v[12:15], v[12:13], off offset:3072
	s_ashr_i32 s15, s50, 31
	s_lshr_b32 s15, s15, 26
	s_add_i32 s15, s50, s15
	s_ashr_i32 s20, s15, 6
	s_ashr_i32 s21, s20, 31
	v_readlane_b32 s98, v253, 20
	v_mbcnt_lo_u32_b32 v200, -1, 0
	v_mbcnt_hi_u32_b32 v200, -1, v200
	v_lshlrev_b32_e32 v200, 2, v200
	s_lshl_b32 s98, s98, 8
	v_add_u32_e32 v200, s98, v200
	v_mov_b32_e32 v201, 0
	s_lshr_b32 s99, s50, 6
	s_mul_i32 s99, s99, 0x6000
	s_add_u32 s100, s94, 0x101000
	s_addc_u32 s101, s95, 0
	s_add_u32 s100, s100, s99
	s_addc_u32 s101, s101, 0
	v_lshl_add_u64 v[202:203], s[100:101], 0, v[200:201]
	global_load_dword v210, v[202:203], off
	global_load_dword v211, v[202:203], off offset:2048
	s_add_u32 s100, s94, 0x100000
	s_addc_u32 s101, s95, 0
	s_add_u32 s100, s100, s99
	s_addc_u32 s101, s101, 0
	v_lshl_add_u64 v[202:203], s[100:101], 0, v[200:201]
	global_load_dword v212, v[202:203], off
	global_load_dword v213, v[202:203], off offset:2048
	s_waitcnt vmcnt(0)
	v_add_f32_e32 v210, 1.0, v210
	v_add_f32_e32 v211, 1.0, v211
	ds_write2st64_b32 v200, v210, v211 offset0:48 offset1:56
	ds_write2st64_b32 v200, v212, v213 offset0:64 offset1:72
	s_add_i32 s14, s14, 32
	s_ashr_i32 s15, s14, 31
	s_lshl_b64 s[20:21], s[20:21], 22
	s_lshl_b64 s[14:15], s[14:15], 12
	s_and_b32 s26, s16, 0xfc0
	v_lshl_add_u64 v[40:41], v[38:39], 0, s[14:15]
	v_lshl_add_u64 v[42:43], v[36:37], 0, s[20:21]
	s_mov_b32 s16, 0
	s_mov_b64 s[14:15], -1
	s_mov_b64 s[22:23], 0
	s_waitcnt lgkmcnt(0)
	s_barrier
	s_branch .LBB0_286

.LBB0_626:
	s_lshl_b32 s62, s61, 6
	s_add_i32 s16, s62, s45
	s_ashr_i32 s17, s16, 31
	s_lshl_b64 s[18:19], s[16:17], 11
	s_lshl_b64 s[28:29], s[16:17], 12
	v_lshl_add_u64 v[12:13], v[82:83], 0, s[28:29]
	v_lshl_add_u64 v[16:17], v[84:85], 0, s[18:19]
	global_load_dwordx4 v[0:3], v[12:13], off
	global_load_dwordx4 v[4:7], v[12:13], off offset:1024
	global_load_dwordx4 v[8:11], v[12:13], off offset:2048
	s_nop 0
	global_load_dwordx4 v[12:15], v[12:13], off offset:3072
	s_nop 0
	global_load_dwordx2 v[32:33], v[16:17], off
	global_load_dwordx2 v[34:35], v[16:17], off offset:512
	global_load_dwordx2 v[36:37], v[16:17], off offset:1024
	global_load_dwordx2 v[38:39], v[16:17], off offset:1536
	v_readlane_b32 s98, v253, 20
	v_mbcnt_lo_u32_b32 v200, -1, 0
	v_mbcnt_hi_u32_b32 v200, -1, v200
	v_lshlrev_b32_e32 v200, 2, v200
	s_lshl_b32 s98, s98, 8
	v_add_u32_e32 v200, s98, v200
	v_mov_b32_e32 v201, 0
	s_lshr_b32 s99, s61, 6
	s_mul_i32 s99, s99, 0x6000
	s_add_u32 s100, s94, 0x102000
	s_addc_u32 s101, s95, 0
	s_add_u32 s100, s100, s99
	s_addc_u32 s101, s101, 0
	v_lshl_add_u64 v[202:203], s[100:101], 0, v[200:201]
	global_load_dword v204, v[202:203], off
	global_load_dword v205, v[202:203], off offset:2048
	v_readlane_b32 s100, v253, 35
	v_readlane_b32 s101, v253, 36
	s_add_u32 s100, s100, 0x0
	s_addc_u32 s101, s101, 0
	v_lshl_add_u64 v[202:203], s[100:101], 0, v[200:201]
	global_load_dword v206, v[202:203], off
	global_load_dword v207, v[202:203], off offset:2048
	v_readlane_b32 s100, v253, 37
	v_readlane_b32 s101, v253, 38
	s_add_u32 s100, s100, 0x0
	s_addc_u32 s101, s101, 0
	v_lshl_add_u64 v[202:203], s[100:101], 0, v[200:201]
	global_load_dword v208, v[202:203], off
	global_load_dword v209, v[202:203], off offset:2048
	s_add_u32 s100, s94, 0x104000
	s_addc_u32 s101, s95, 0
	s_add_u32 s100, s100, s99
	s_addc_u32 s101, s101, 0
	v_lshl_add_u64 v[202:203], s[100:101], 0, v[200:201]
	global_load_dword v210, v[202:203], off
	global_load_dword v211, v[202:203], off offset:2048
	s_add_u32 s100, s94, 0x103000
	s_addc_u32 s101, s95, 0
	s_add_u32 s100, s100, s99
	s_addc_u32 s101, s101, 0
	v_lshl_add_u64 v[202:203], s[100:101], 0, v[200:201]
	global_load_dword v212, v[202:203], off
	global_load_dword v213, v[202:203], off offset:2048
	s_waitcnt vmcnt(0)
	ds_write2st64_b32 v200, v204, v205 offset1:8
	ds_write2st64_b32 v200, v206, v207 offset0:16 offset1:24
	ds_write2st64_b32 v200, v208, v209 offset0:32 offset1:40
	v_add_f32_e32 v210, 1.0, v210
	v_add_f32_e32 v211, 1.0, v211
	ds_write2st64_b32 v200, v210, v211 offset0:48 offset1:56
	ds_write2st64_b32 v200, v212, v213 offset0:64 offset1:72
	s_add_i32 s16, s16, 32
	s_ashr_i32 s17, s16, 31
	s_lshl_b64 s[18:19], s[16:17], 11
	s_lshl_b64 s[16:17], s[16:17], 12
	v_lshl_add_u64 v[90:91], v[82:83], 0, s[16:17]
	v_lshl_add_u64 v[92:93], v[84:85], 0, s[18:19]
	s_mov_b32 s33, 0
	s_mov_b64 s[16:17], -1
	s_mov_b64 s[28:29], 0
	s_waitcnt lgkmcnt(0)
	s_barrier
	s_branch .LBB0_642

.LBB0_1140:
	v_lshl_add_u32 v8, s59, 8, v35
	v_ashrrev_i32_e32 v9, 31, v8
	v_lshlrev_b64 v[8:9], 2, v[8:9]
	s_waitcnt vmcnt(27)
	v_lshl_add_u64 v[10:11], s[16:17], 0, v[8:9]
	global_load_dword v47, v[10:11], off
	s_lshl_b32 s60, s59, 6
	s_add_i32 s12, s60, s50
	s_ashr_i32 s13, s12, 31
	s_lshl_b64 s[28:29], s[12:13], 11
	s_waitcnt vmcnt(25)
	v_lshl_add_u64 v[16:17], v[2:3], 0, s[28:29]
	v_lshl_add_u64 v[8:9], s[14:15], 0, v[8:9]
	global_load_dword v48, v[8:9], off
	global_load_dwordx2 v[10:11], v[16:17], off
	global_load_dwordx2 v[12:13], v[16:17], off offset:512
	s_waitcnt vmcnt(3)
	v_readlane_b32 s28, v47, 0
	v_readlane_b32 s30, v47, 1
	v_readlane_b32 s34, v47, 2
	v_readlane_b32 s36, v47, 3
	s_ashr_i32 s29, s28, 31
	s_ashr_i32 s31, s30, 31
	s_ashr_i32 s35, s34, 31
	s_ashr_i32 s37, s36, 31
	s_lshl_b64 s[28:29], s[28:29], 10
	s_lshl_b64 s[30:31], s[30:31], 10
	s_lshl_b64 s[34:35], s[34:35], 10
	s_lshl_b64 s[36:37], s[36:37], 10
	v_lshl_add_u64 v[8:9], v[4:5], 0, s[28:29]
	v_lshl_add_u64 v[18:19], v[4:5], 0, s[30:31]
	v_lshl_add_u64 v[20:21], v[4:5], 0, s[34:35]
	v_lshl_add_u64 v[22:23], v[4:5], 0, s[36:37]
	global_load_dwordx2 v[14:15], v[16:17], off offset:1024
	s_nop 0
	global_load_dwordx2 v[16:17], v[16:17], off offset:1536
	s_nop 0
	global_load_dword v53, v[8:9], off
	global_load_dword v54, v[8:9], off offset:256
	global_load_dword v55, v[8:9], off offset:512
	global_load_dword v56, v[8:9], off offset:768
	global_load_dword v49, v[18:19], off
	global_load_dword v50, v[18:19], off offset:256
	global_load_dword v51, v[18:19], off offset:512
	global_load_dword v52, v[18:19], off offset:768
	global_load_dword v57, v[20:21], off
	global_load_dword v58, v[20:21], off offset:256
	global_load_dword v59, v[20:21], off offset:512
	global_load_dword v60, v[20:21], off offset:768
	global_load_dword v61, v[22:23], off
	global_load_dword v62, v[22:23], off offset:256
	global_load_dword v63, v[22:23], off offset:512
	global_load_dword v64, v[22:23], off offset:768
	s_waitcnt vmcnt(20)
	v_readlane_b32 s31, v48, 0
	v_readlane_b32 s30, v48, 1
	v_readlane_b32 s29, v48, 2
	v_readlane_b32 s28, v48, 3
	v_readlane_b32 s98, v253, 20
	v_mbcnt_lo_u32_b32 v200, -1, 0
	v_mbcnt_hi_u32_b32 v200, -1, v200
	v_lshlrev_b32_e32 v200, 2, v200
	s_lshl_b32 s98, s98, 8
	v_add_u32_e32 v200, s98, v200
	v_mov_b32_e32 v201, 0
	s_lshr_b32 s99, s59, 6
	s_mul_i32 s99, s99, 0x6000
	s_add_u32 s100, s94, 0x105000
	s_addc_u32 s101, s95, 0
	s_add_u32 s100, s100, s99
	s_addc_u32 s101, s101, 0
	v_lshl_add_u64 v[202:203], s[100:101], 0, v[200:201]
	global_load_dword v204, v[202:203], off
	global_load_dword v205, v[202:203], off offset:2048
	v_readlane_b32 s100, v253, 35
	v_readlane_b32 s101, v253, 36
	s_add_u32 s100, s100, 0x1000
	s_addc_u32 s101, s101, 0
	v_lshl_add_u64 v[202:203], s[100:101], 0, v[200:201]
	global_load_dword v206, v[202:203], off
	global_load_dword v207, v[202:203], off offset:2048
	v_readlane_b32 s100, v253, 37
	v_readlane_b32 s101, v253, 38
	s_add_u32 s100, s100, 0x1000
	s_addc_u32 s101, s101, 0
	v_lshl_add_u64 v[202:203], s[100:101], 0, v[200:201]
	global_load_dword v208, v[202:203], off
	global_load_dword v209, v[202:203], off offset:2048
	s_add_u32 s100, s94, 0x119000
	s_addc_u32 s101, s95, 0
	s_add_u32 s100, s100, s99
	s_addc_u32 s101, s101, 0
	v_lshl_add_u64 v[202:203], s[100:101], 0, v[200:201]
	global_load_dword v210, v[202:203], off
	global_load_dword v211, v[202:203], off offset:2048
	s_add_u32 s100, s94, 0x118000
	s_addc_u32 s101, s95, 0
	s_add_u32 s100, s100, s99
	s_addc_u32 s101, s101, 0
	v_lshl_add_u64 v[202:203], s[100:101], 0, v[200:201]
	global_load_dword v212, v[202:203], off
	global_load_dword v213, v[202:203], off offset:2048
	s_waitcnt vmcnt(0)
	ds_write2st64_b32 v200, v204, v205 offset1:8
	ds_write2st64_b32 v200, v206, v207 offset0:16 offset1:24
	ds_write2st64_b32 v200, v208, v209 offset0:32 offset1:40
	v_add_f32_e32 v210, 1.0, v210
	v_add_f32_e32 v211, 1.0, v211
	ds_write2st64_b32 v200, v210, v211 offset0:48 offset1:56
	ds_write2st64_b32 v200, v212, v213 offset0:64 offset1:72
	s_add_i32 s12, s12, 32
	s_ashr_i32 s13, s12, 31
	v_mov_b64_e32 v[8:9], s[24:25]
	s_lshl_b64 s[12:13], s[12:13], 11
	v_pk_mul_f32 v[26:27], s[30:31], v[8:9] op_sel_hi:[1,0]
	v_pk_mul_f32 v[28:29], s[28:29], v[8:9] op_sel_hi:[1,0]
	v_lshl_add_u64 v[8:9], v[2:3], 0, s[12:13]
	s_mov_b32 s34, 0
	s_mov_b64 s[12:13], -1
	s_mov_b64 s[30:31], 0
	s_waitcnt lgkmcnt(0)
	s_barrier
	s_branch .LBB0_1154

.LBB0_1449:
	s_lshl_b32 s67, s66, 6
	s_add_i32 s16, s67, s51
	s_ashr_i32 s17, s16, 31
	s_lshl_b64 s[18:19], s[16:17], 11
	v_lshl_add_u64 v[6:7], v[82:83], 0, s[18:19]
	v_lshl_add_u64 v[14:15], v[84:85], 0, s[18:19]
	global_load_dwordx2 v[0:1], v[6:7], off
	global_load_dwordx2 v[2:3], v[6:7], off offset:512
	global_load_dwordx2 v[4:5], v[6:7], off offset:1024
	s_nop 0
	global_load_dwordx2 v[6:7], v[6:7], off offset:1536
	s_nop 0
	global_load_dwordx2 v[8:9], v[14:15], off
	global_load_dwordx2 v[10:11], v[14:15], off offset:512
	global_load_dwordx2 v[12:13], v[14:15], off offset:1024
	s_nop 0
	global_load_dwordx2 v[14:15], v[14:15], off offset:1536
	v_readlane_b32 s98, v253, 20
	v_mbcnt_lo_u32_b32 v200, -1, 0
	v_mbcnt_hi_u32_b32 v200, -1, v200
	v_lshlrev_b32_e32 v200, 2, v200
	s_lshl_b32 s98, s98, 8
	v_add_u32_e32 v200, s98, v200
	v_mov_b32_e32 v201, 0
	s_lshr_b32 s99, s66, 6
	s_mul_i32 s99, s99, 0x6000
	s_add_u32 s100, s94, 0x11a000
	s_addc_u32 s101, s95, 0
	s_add_u32 s100, s100, s99
	s_addc_u32 s101, s101, 0
	v_lshl_add_u64 v[202:203], s[100:101], 0, v[200:201]
	global_load_dword v204, v[202:203], off
	global_load_dword v205, v[202:203], off offset:2048
	v_readlane_b32 s100, v253, 35
	v_readlane_b32 s101, v253, 36
	s_add_u32 s100, s100, 0x2000
	s_addc_u32 s101, s101, 0
	v_lshl_add_u64 v[202:203], s[100:101], 0, v[200:201]
	global_load_dword v206, v[202:203], off
	global_load_dword v207, v[202:203], off offset:2048
	v_readlane_b32 s100, v253, 37
	v_readlane_b32 s101, v253, 38
	s_add_u32 s100, s100, 0x2000
	s_addc_u32 s101, s101, 0
	v_lshl_add_u64 v[202:203], s[100:101], 0, v[200:201]
	global_load_dword v208, v[202:203], off
	global_load_dword v209, v[202:203], off offset:2048
	s_add_u32 s100, s94, 0x11c000
	s_addc_u32 s101, s95, 0
	s_add_u32 s100, s100, s99
	s_addc_u32 s101, s101, 0
	v_lshl_add_u64 v[202:203], s[100:101], 0, v[200:201]
	global_load_dword v210, v[202:203], off
	global_load_dword v211, v[202:203], off offset:2048
	s_add_u32 s100, s94, 0x11b000
	s_addc_u32 s101, s95, 0
	s_add_u32 s100, s100, s99
	s_addc_u32 s101, s101, 0
	v_lshl_add_u64 v[202:203], s[100:101], 0, v[200:201]
	global_load_dword v212, v[202:203], off
	global_load_dword v213, v[202:203], off offset:2048
	s_waitcnt vmcnt(0)
	ds_write2st64_b32 v200, v204, v205 offset1:8
	ds_write2st64_b32 v200, v206, v207 offset0:16 offset1:24
	ds_write2st64_b32 v200, v208, v209 offset0:32 offset1:40
	v_add_f32_e32 v210, 1.0, v210
	v_add_f32_e32 v211, 1.0, v211
	ds_write2st64_b32 v200, v210, v211 offset0:48 offset1:56
	ds_write2st64_b32 v200, v212, v213 offset0:64 offset1:72
	s_add_i32 s16, s16, 32
	s_ashr_i32 s17, s16, 31
	s_lshl_b64 s[16:17], s[16:17], 11
	v_lshl_add_u64 v[16:17], v[82:83], 0, s[16:17]
	v_lshl_add_u64 v[18:19], v[84:85], 0, s[16:17]
	s_mov_b32 s33, 0
	s_mov_b64 s[16:17], -1
	s_mov_b64 s[36:37], 0
	s_waitcnt lgkmcnt(0)
	s_barrier
	s_branch .LBB0_1465

.LBB0_1963:
	v_lshl_add_u32 v8, s64, 8, v38
	v_ashrrev_i32_e32 v9, 31, v8
	v_lshlrev_b64 v[8:9], 2, v[8:9]
	s_waitcnt vmcnt(23)
	v_lshl_add_u64 v[10:11], s[18:19], 0, v[8:9]
	global_load_dword v48, v[10:11], off
	s_lshl_b32 s65, s64, 6
	s_add_i32 s14, s65, s54
	s_ashr_i32 s15, s14, 31
	s_lshl_b64 s[34:35], s[14:15], 11
	s_waitcnt vmcnt(21)
	v_lshl_add_u64 v[16:17], v[2:3], 0, s[34:35]
	v_lshl_add_u64 v[8:9], s[16:17], 0, v[8:9]
	global_load_dword v49, v[8:9], off
	global_load_dwordx2 v[10:11], v[16:17], off
	global_load_dwordx2 v[12:13], v[16:17], off offset:512
	s_ashr_i32 s15, s64, 31
	s_lshr_b32 s15, s15, 26
	s_add_i32 s15, s64, s15
	s_ashr_i32 s15, s15, 6
	s_waitcnt vmcnt(3)
	v_readlane_b32 s34, v48, 0
	v_readlane_b32 s36, v48, 1
	v_readlane_b32 s38, v48, 2
	v_readlane_b32 s40, v48, 3
	s_ashr_i32 s35, s34, 31
	s_ashr_i32 s37, s36, 31
	s_ashr_i32 s39, s38, 31
	s_ashr_i32 s41, s40, 31
	s_lshl_b64 s[34:35], s[34:35], 10
	s_lshl_b64 s[36:37], s[36:37], 10
	s_lshl_b64 s[38:39], s[38:39], 10
	s_lshl_b64 s[40:41], s[40:41], 10
	v_lshl_add_u64 v[8:9], v[4:5], 0, s[34:35]
	v_lshl_add_u64 v[18:19], v[4:5], 0, s[36:37]
	v_lshl_add_u64 v[20:21], v[4:5], 0, s[38:39]
	v_lshl_add_u64 v[22:23], v[4:5], 0, s[40:41]
	global_load_dwordx2 v[14:15], v[16:17], off offset:1024
	s_nop 0
	global_load_dwordx2 v[16:17], v[16:17], off offset:1536
	s_nop 0
	global_load_dword v54, v[8:9], off
	global_load_dword v55, v[8:9], off offset:256
	global_load_dword v56, v[8:9], off offset:512
	global_load_dword v57, v[8:9], off offset:768
	global_load_dword v53, v[18:19], off
	global_load_dword v52, v[18:19], off offset:256
	global_load_dword v51, v[18:19], off offset:512
	global_load_dword v50, v[18:19], off offset:768
	global_load_dword v65, v[20:21], off
	global_load_dword v64, v[20:21], off offset:256
	global_load_dword v63, v[20:21], off offset:512
	global_load_dword v62, v[20:21], off offset:768
	global_load_dword v61, v[22:23], off
	global_load_dword v60, v[22:23], off offset:256
	global_load_dword v59, v[22:23], off offset:512
	global_load_dword v58, v[22:23], off offset:768
	s_waitcnt vmcnt(20)
	v_readlane_b32 s37, v49, 0
	v_readlane_b32 s36, v49, 1
	v_readlane_b32 s35, v49, 2
	v_readlane_b32 s34, v49, 3
	v_readlane_b32 s98, v253, 20
	v_mbcnt_lo_u32_b32 v200, -1, 0
	v_mbcnt_hi_u32_b32 v200, -1, v200
	v_lshlrev_b32_e32 v200, 2, v200
	s_lshl_b32 s98, s98, 8
	v_add_u32_e32 v200, s98, v200
	v_mov_b32_e32 v201, 0
	s_lshr_b32 s99, s64, 6
	s_mul_i32 s99, s99, 0x6000
	s_add_u32 s100, s94, 0x11d000
	s_addc_u32 s101, s95, 0
	s_add_u32 s100, s100, s99
	s_addc_u32 s101, s101, 0
	v_lshl_add_u64 v[202:203], s[100:101], 0, v[200:201]
	global_load_dword v204, v[202:203], off
	global_load_dword v205, v[202:203], off offset:2048
	v_readlane_b32 s100, v253, 35
	v_readlane_b32 s101, v253, 36
	s_add_u32 s100, s100, 0x3000
	s_addc_u32 s101, s101, 0
	v_lshl_add_u64 v[202:203], s[100:101], 0, v[200:201]
	global_load_dword v206, v[202:203], off
	global_load_dword v207, v[202:203], off offset:2048
	v_readlane_b32 s100, v253, 37
	v_readlane_b32 s101, v253, 38
	s_add_u32 s100, s100, 0x3000
	s_addc_u32 s101, s101, 0
	v_lshl_add_u64 v[202:203], s[100:101], 0, v[200:201]
	global_load_dword v208, v[202:203], off
	global_load_dword v209, v[202:203], off offset:2048
	s_add_u32 s100, s94, 0x131000
	s_addc_u32 s101, s95, 0
	s_add_u32 s100, s100, s99
	s_addc_u32 s101, s101, 0
	v_lshl_add_u64 v[202:203], s[100:101], 0, v[200:201]
	global_load_dword v210, v[202:203], off
	global_load_dword v211, v[202:203], off offset:2048
	s_add_u32 s100, s94, 0x130000
	s_addc_u32 s101, s95, 0
	s_add_u32 s100, s100, s99
	s_addc_u32 s101, s101, 0
	v_lshl_add_u64 v[202:203], s[100:101], 0, v[200:201]
	global_load_dword v212, v[202:203], off
	global_load_dword v213, v[202:203], off offset:2048
	s_waitcnt vmcnt(0)
	ds_write2st64_b32 v200, v204, v205 offset1:8
	ds_write2st64_b32 v200, v206, v207 offset0:16 offset1:24
	ds_write2st64_b32 v200, v208, v209 offset0:32 offset1:40
	v_add_f32_e32 v210, 1.0, v210
	v_add_f32_e32 v211, 1.0, v211
	ds_write2st64_b32 v200, v210, v211 offset0:48 offset1:56
	ds_write2st64_b32 v200, v212, v213 offset0:64 offset1:72
	s_add_i32 s14, s14, 32
	s_lshl_b32 s45, s15, 8
	s_ashr_i32 s15, s14, 31
	v_mov_b64_e32 v[8:9], s[28:29]
	s_lshl_b64 s[14:15], s[14:15], 11
	v_pk_mul_f32 v[26:27], s[36:37], v[8:9] op_sel_hi:[1,0]
	v_pk_mul_f32 v[28:29], s[34:35], v[8:9] op_sel_hi:[1,0]
	s_and_b32 s44, s65, 0xfc0
	v_lshl_add_u64 v[8:9], v[2:3], 0, s[14:15]
	s_mov_b32 s38, 0
	s_mov_b64 s[14:15], -1
	s_mov_b64 s[36:37], 0
	s_waitcnt lgkmcnt(0)
	s_barrier
	s_branch .LBB0_1977

.LBB0_2357:
	s_lshl_b32 s67, s66, 6
	s_add_i32 s16, s67, s51
	s_ashr_i32 s17, s16, 31
	s_lshl_b64 s[18:19], s[16:17], 11
	v_lshl_add_u64 v[6:7], v[82:83], 0, s[18:19]
	v_lshl_add_u64 v[14:15], v[84:85], 0, s[18:19]
	global_load_dwordx2 v[0:1], v[6:7], off
	global_load_dwordx2 v[2:3], v[6:7], off offset:512
	global_load_dwordx2 v[4:5], v[6:7], off offset:1024
	s_nop 0
	global_load_dwordx2 v[6:7], v[6:7], off offset:1536
	s_nop 0
	global_load_dwordx2 v[8:9], v[14:15], off
	global_load_dwordx2 v[10:11], v[14:15], off offset:512
	global_load_dwordx2 v[12:13], v[14:15], off offset:1024
	s_nop 0
	global_load_dwordx2 v[14:15], v[14:15], off offset:1536
	v_readlane_b32 s98, v253, 20
	v_mbcnt_lo_u32_b32 v200, -1, 0
	v_mbcnt_hi_u32_b32 v200, -1, v200
	v_lshlrev_b32_e32 v200, 2, v200
	s_lshl_b32 s98, s98, 8
	v_add_u32_e32 v200, s98, v200
	v_mov_b32_e32 v201, 0
	s_lshr_b32 s99, s66, 6
	s_mul_i32 s99, s99, 0x6000
	s_add_u32 s100, s94, 0x132000
	s_addc_u32 s101, s95, 0
	s_add_u32 s100, s100, s99
	s_addc_u32 s101, s101, 0
	v_lshl_add_u64 v[202:203], s[100:101], 0, v[200:201]
	global_load_dword v204, v[202:203], off
	global_load_dword v205, v[202:203], off offset:2048
	v_readlane_b32 s100, v253, 35
	v_readlane_b32 s101, v253, 36
	s_add_u32 s100, s100, 0x4000
	s_addc_u32 s101, s101, 0
	v_lshl_add_u64 v[202:203], s[100:101], 0, v[200:201]
	global_load_dword v206, v[202:203], off
	global_load_dword v207, v[202:203], off offset:2048
	v_readlane_b32 s100, v253, 37
	v_readlane_b32 s101, v253, 38
	s_add_u32 s100, s100, 0x4000
	s_addc_u32 s101, s101, 0
	v_lshl_add_u64 v[202:203], s[100:101], 0, v[200:201]
	global_load_dword v208, v[202:203], off
	global_load_dword v209, v[202:203], off offset:2048
	s_add_u32 s100, s94, 0x134000
	s_addc_u32 s101, s95, 0
	s_add_u32 s100, s100, s99
	s_addc_u32 s101, s101, 0
	v_lshl_add_u64 v[202:203], s[100:101], 0, v[200:201]
	global_load_dword v210, v[202:203], off
	global_load_dword v211, v[202:203], off offset:2048
	s_add_u32 s100, s94, 0x133000
	s_addc_u32 s101, s95, 0
	s_add_u32 s100, s100, s99
	s_addc_u32 s101, s101, 0
	v_lshl_add_u64 v[202:203], s[100:101], 0, v[200:201]
	global_load_dword v212, v[202:203], off
	global_load_dword v213, v[202:203], off offset:2048
	s_waitcnt vmcnt(0)
	ds_write2st64_b32 v200, v204, v205 offset1:8
	ds_write2st64_b32 v200, v206, v207 offset0:16 offset1:24
	ds_write2st64_b32 v200, v208, v209 offset0:32 offset1:40
	v_add_f32_e32 v210, 1.0, v210
	v_add_f32_e32 v211, 1.0, v211
	ds_write2st64_b32 v200, v210, v211 offset0:48 offset1:56
	ds_write2st64_b32 v200, v212, v213 offset0:64 offset1:72
	s_add_i32 s16, s16, 32
	s_ashr_i32 s17, s16, 31
	s_lshl_b64 s[16:17], s[16:17], 11
	v_lshl_add_u64 v[16:17], v[82:83], 0, s[16:17]
	v_lshl_add_u64 v[18:19], v[84:85], 0, s[16:17]
	s_mov_b32 s33, 0
	s_mov_b64 s[16:17], -1
	s_mov_b64 s[36:37], 0
	s_waitcnt lgkmcnt(0)
	s_barrier
	s_branch .LBB0_2373

.LBB0_2871:
	v_lshl_add_u32 v8, s59, 8, v35
	v_ashrrev_i32_e32 v9, 31, v8
	v_lshlrev_b64 v[8:9], 2, v[8:9]
	s_waitcnt vmcnt(27)
	v_lshl_add_u64 v[10:11], s[16:17], 0, v[8:9]
	global_load_dword v47, v[10:11], off
	s_lshl_b32 s60, s59, 6
	s_add_i32 s12, s60, s50
	s_ashr_i32 s13, s12, 31
	s_lshl_b64 s[28:29], s[12:13], 11
	s_waitcnt vmcnt(25)
	v_lshl_add_u64 v[16:17], v[2:3], 0, s[28:29]
	v_lshl_add_u64 v[8:9], s[14:15], 0, v[8:9]
	global_load_dword v48, v[8:9], off
	global_load_dwordx2 v[10:11], v[16:17], off
	global_load_dwordx2 v[12:13], v[16:17], off offset:512
	s_waitcnt vmcnt(3)
	v_readlane_b32 s28, v47, 0
	v_readlane_b32 s30, v47, 1
	v_readlane_b32 s34, v47, 2
	v_readlane_b32 s36, v47, 3
	s_ashr_i32 s29, s28, 31
	s_ashr_i32 s31, s30, 31
	s_ashr_i32 s35, s34, 31
	s_ashr_i32 s37, s36, 31
	s_lshl_b64 s[28:29], s[28:29], 10
	s_lshl_b64 s[30:31], s[30:31], 10
	s_lshl_b64 s[34:35], s[34:35], 10
	s_lshl_b64 s[36:37], s[36:37], 10
	v_lshl_add_u64 v[8:9], v[4:5], 0, s[28:29]
	v_lshl_add_u64 v[18:19], v[4:5], 0, s[30:31]
	v_lshl_add_u64 v[20:21], v[4:5], 0, s[34:35]
	v_lshl_add_u64 v[22:23], v[4:5], 0, s[36:37]
	global_load_dwordx2 v[14:15], v[16:17], off offset:1024
	s_nop 0
	global_load_dwordx2 v[16:17], v[16:17], off offset:1536
	s_nop 0
	global_load_dword v53, v[8:9], off
	global_load_dword v54, v[8:9], off offset:256
	global_load_dword v55, v[8:9], off offset:512
	global_load_dword v56, v[8:9], off offset:768
	global_load_dword v49, v[18:19], off
	global_load_dword v50, v[18:19], off offset:256
	global_load_dword v51, v[18:19], off offset:512
	global_load_dword v52, v[18:19], off offset:768
	global_load_dword v57, v[20:21], off
	global_load_dword v58, v[20:21], off offset:256
	global_load_dword v59, v[20:21], off offset:512
	global_load_dword v60, v[20:21], off offset:768
	global_load_dword v61, v[22:23], off
	global_load_dword v62, v[22:23], off offset:256
	global_load_dword v63, v[22:23], off offset:512
	global_load_dword v64, v[22:23], off offset:768
	s_waitcnt vmcnt(20)
	v_readlane_b32 s31, v48, 0
	v_readlane_b32 s30, v48, 1
	v_readlane_b32 s29, v48, 2
	v_readlane_b32 s28, v48, 3
	v_readlane_b32 s98, v253, 20
	v_mbcnt_lo_u32_b32 v200, -1, 0
	v_mbcnt_hi_u32_b32 v200, -1, v200
	v_lshlrev_b32_e32 v200, 2, v200
	s_lshl_b32 s98, s98, 8
	v_add_u32_e32 v200, s98, v200
	v_mov_b32_e32 v201, 0
	s_lshr_b32 s99, s59, 6
	s_mul_i32 s99, s99, 0x6000
	s_add_u32 s100, s94, 0x135000
	s_addc_u32 s101, s95, 0
	s_add_u32 s100, s100, s99
	s_addc_u32 s101, s101, 0
	v_lshl_add_u64 v[202:203], s[100:101], 0, v[200:201]
	global_load_dword v204, v[202:203], off
	global_load_dword v205, v[202:203], off offset:2048
	v_readlane_b32 s100, v253, 35
	v_readlane_b32 s101, v253, 36
	s_add_u32 s100, s100, 0x5000
	s_addc_u32 s101, s101, 0
	v_lshl_add_u64 v[202:203], s[100:101], 0, v[200:201]
	global_load_dword v206, v[202:203], off
	global_load_dword v207, v[202:203], off offset:2048
	v_readlane_b32 s100, v253, 37
	v_readlane_b32 s101, v253, 38
	s_add_u32 s100, s100, 0x5000
	s_addc_u32 s101, s101, 0
	v_lshl_add_u64 v[202:203], s[100:101], 0, v[200:201]
	global_load_dword v208, v[202:203], off
	global_load_dword v209, v[202:203], off offset:2048
	s_add_u32 s100, s94, 0x149000
	s_addc_u32 s101, s95, 0
	s_add_u32 s100, s100, s99
	s_addc_u32 s101, s101, 0
	v_lshl_add_u64 v[202:203], s[100:101], 0, v[200:201]
	global_load_dword v210, v[202:203], off
	global_load_dword v211, v[202:203], off offset:2048
	s_add_u32 s100, s94, 0x148000
	s_addc_u32 s101, s95, 0
	s_add_u32 s100, s100, s99
	s_addc_u32 s101, s101, 0
	v_lshl_add_u64 v[202:203], s[100:101], 0, v[200:201]
	global_load_dword v212, v[202:203], off
	global_load_dword v213, v[202:203], off offset:2048
	s_waitcnt vmcnt(0)
	ds_write2st64_b32 v200, v204, v205 offset1:8
	ds_write2st64_b32 v200, v206, v207 offset0:16 offset1:24
	ds_write2st64_b32 v200, v208, v209 offset0:32 offset1:40
	v_add_f32_e32 v210, 1.0, v210
	v_add_f32_e32 v211, 1.0, v211
	ds_write2st64_b32 v200, v210, v211 offset0:48 offset1:56
	ds_write2st64_b32 v200, v212, v213 offset0:64 offset1:72
	s_add_i32 s12, s12, 32
	s_ashr_i32 s13, s12, 31
	v_mov_b64_e32 v[8:9], s[24:25]
	s_lshl_b64 s[12:13], s[12:13], 11
	v_pk_mul_f32 v[26:27], s[30:31], v[8:9] op_sel_hi:[1,0]
	v_pk_mul_f32 v[28:29], s[28:29], v[8:9] op_sel_hi:[1,0]
	v_lshl_add_u64 v[8:9], v[2:3], 0, s[12:13]
	s_mov_b32 s34, 0
	s_mov_b64 s[12:13], -1
	s_mov_b64 s[30:31], 0
	s_waitcnt lgkmcnt(0)
	s_barrier
	s_branch .LBB0_2885

.LBB0_3304:
	s_lshl_b32 s96, s91, 6
	s_add_i32 s16, s96, s51
	s_ashr_i32 s17, s16, 31
	s_lshl_b64 s[18:19], s[16:17], 11
	v_lshl_add_u64 v[6:7], v[82:83], 0, s[18:19]
	v_lshl_add_u64 v[14:15], v[84:85], 0, s[18:19]
	global_load_dwordx2 v[0:1], v[6:7], off
	global_load_dwordx2 v[2:3], v[6:7], off offset:512
	global_load_dwordx2 v[4:5], v[6:7], off offset:1024
	s_nop 0
	global_load_dwordx2 v[6:7], v[6:7], off offset:1536
	s_nop 0
	global_load_dwordx2 v[8:9], v[14:15], off
	global_load_dwordx2 v[10:11], v[14:15], off offset:512
	global_load_dwordx2 v[12:13], v[14:15], off offset:1024
	s_nop 0
	global_load_dwordx2 v[14:15], v[14:15], off offset:1536
	v_readlane_b32 s98, v253, 20
	v_mbcnt_lo_u32_b32 v200, -1, 0
	v_mbcnt_hi_u32_b32 v200, -1, v200
	v_lshlrev_b32_e32 v200, 2, v200
	s_lshl_b32 s98, s98, 8
	v_add_u32_e32 v200, s98, v200
	v_mov_b32_e32 v201, 0
	s_lshr_b32 s99, s91, 6
	s_mul_i32 s99, s99, 0x6000
	s_add_u32 s100, s94, 0x14a000
	s_addc_u32 s101, s95, 0
	s_add_u32 s100, s100, s99
	s_addc_u32 s101, s101, 0
	v_lshl_add_u64 v[202:203], s[100:101], 0, v[200:201]
	global_load_dword v204, v[202:203], off
	global_load_dword v205, v[202:203], off offset:2048
	v_readlane_b32 s100, v253, 35
	v_readlane_b32 s101, v253, 36
	s_add_u32 s100, s100, 0x6000
	s_addc_u32 s101, s101, 0
	v_lshl_add_u64 v[202:203], s[100:101], 0, v[200:201]
	global_load_dword v206, v[202:203], off
	global_load_dword v207, v[202:203], off offset:2048
	v_readlane_b32 s100, v253, 37
	v_readlane_b32 s101, v253, 38
	s_add_u32 s100, s100, 0x6000
	s_addc_u32 s101, s101, 0
	v_lshl_add_u64 v[202:203], s[100:101], 0, v[200:201]
	global_load_dword v208, v[202:203], off
	global_load_dword v209, v[202:203], off offset:2048
	s_add_u32 s100, s94, 0x14c000
	s_addc_u32 s101, s95, 0
	s_add_u32 s100, s100, s99
	s_addc_u32 s101, s101, 0
	v_lshl_add_u64 v[202:203], s[100:101], 0, v[200:201]
	global_load_dword v210, v[202:203], off
	global_load_dword v211, v[202:203], off offset:2048
	s_add_u32 s100, s94, 0x14b000
	s_addc_u32 s101, s95, 0
	s_add_u32 s100, s100, s99
	s_addc_u32 s101, s101, 0
	v_lshl_add_u64 v[202:203], s[100:101], 0, v[200:201]
	global_load_dword v212, v[202:203], off
	global_load_dword v213, v[202:203], off offset:2048
	s_waitcnt vmcnt(0)
	ds_write2st64_b32 v200, v204, v205 offset1:8
	ds_write2st64_b32 v200, v206, v207 offset0:16 offset1:24
	ds_write2st64_b32 v200, v208, v209 offset0:32 offset1:40
	v_add_f32_e32 v210, 1.0, v210
	v_add_f32_e32 v211, 1.0, v211
	ds_write2st64_b32 v200, v210, v211 offset0:48 offset1:56
	ds_write2st64_b32 v200, v212, v213 offset0:64 offset1:72
	s_add_i32 s16, s16, 32
	s_ashr_i32 s17, s16, 31
	s_lshl_b64 s[16:17], s[16:17], 11
	v_lshl_add_u64 v[16:17], v[82:83], 0, s[16:17]
	v_lshl_add_u64 v[18:19], v[84:85], 0, s[16:17]
	s_mov_b32 s33, 0
	s_mov_b64 s[16:17], -1
	s_mov_b64 s[36:37], 0
	s_waitcnt lgkmcnt(0)
	s_barrier
	s_branch .LBB0_3320

.LBB0_3796:
	v_lshl_add_u32 v0, s88, 8, v82
	v_ashrrev_i32_e32 v1, 31, v0
	v_lshlrev_b64 v[0:1], 2, v[0:1]
	v_lshl_add_u64 v[2:3], s[14:15], 0, v[0:1]
	global_load_dword v89, v[2:3], off
	s_lshl_b32 s33, s88, 6
	s_add_i32 s10, s33, s44
	s_ashr_i32 s11, s10, 31
	s_lshl_b64 s[28:29], s[10:11], 11
	v_lshl_add_u64 v[2:3], v[50:51], 0, s[28:29]
	v_lshl_add_u64 v[0:1], s[12:13], 0, v[0:1]
	global_load_dword v90, v[0:1], off
	global_load_dwordx2 v[60:61], v[2:3], off
	global_load_dwordx2 v[62:63], v[2:3], off offset:512
	s_waitcnt vmcnt(3)
	v_readlane_b32 s28, v89, 0
	v_readlane_b32 s30, v89, 1
	v_readlane_b32 s34, v89, 2
	v_readlane_b32 s36, v89, 3
	s_ashr_i32 s29, s28, 31
	s_ashr_i32 s31, s30, 31
	s_ashr_i32 s35, s34, 31
	s_ashr_i32 s37, s36, 31
	s_lshl_b64 s[28:29], s[28:29], 10
	s_lshl_b64 s[30:31], s[30:31], 10
	s_lshl_b64 s[34:35], s[34:35], 10
	s_lshl_b64 s[36:37], s[36:37], 10
	v_lshl_add_u64 v[0:1], v[52:53], 0, s[28:29]
	v_lshl_add_u64 v[4:5], v[52:53], 0, s[30:31]
	v_lshl_add_u64 v[6:7], v[52:53], 0, s[34:35]
	v_lshl_add_u64 v[8:9], v[52:53], 0, s[36:37]
	global_load_dwordx2 v[64:65], v[2:3], off offset:1024
	global_load_dwordx2 v[66:67], v[2:3], off offset:1536
	global_load_dword v95, v[0:1], off
	global_load_dword v96, v[0:1], off offset:256
	global_load_dword v97, v[0:1], off offset:512
	global_load_dword v98, v[0:1], off offset:768
	global_load_dword v91, v[4:5], off
	global_load_dword v92, v[4:5], off offset:256
	global_load_dword v93, v[4:5], off offset:512
	global_load_dword v94, v[4:5], off offset:768
	global_load_dword v99, v[6:7], off
	global_load_dword v100, v[6:7], off offset:256
	global_load_dword v101, v[6:7], off offset:512
	global_load_dword v102, v[6:7], off offset:768
	global_load_dword v103, v[8:9], off
	global_load_dword v104, v[8:9], off offset:256
	global_load_dword v105, v[8:9], off offset:512
	global_load_dword v106, v[8:9], off offset:768
	s_waitcnt vmcnt(20)
	v_readlane_b32 s31, v90, 0
	v_readlane_b32 s30, v90, 1
	v_readlane_b32 s29, v90, 2
	v_readlane_b32 s28, v90, 3
	v_readlane_b32 s98, v253, 20
	v_mbcnt_lo_u32_b32 v200, -1, 0
	v_mbcnt_hi_u32_b32 v200, -1, v200
	v_lshlrev_b32_e32 v200, 2, v200
	s_lshl_b32 s98, s98, 8
	v_add_u32_e32 v200, s98, v200
	v_mov_b32_e32 v201, 0
	s_lshr_b32 s99, s88, 6
	s_mul_i32 s99, s99, 0x6000
	s_add_u32 s100, s94, 0x14d000
	s_addc_u32 s101, s95, 0
	s_add_u32 s100, s100, s99
	s_addc_u32 s101, s101, 0
	v_lshl_add_u64 v[202:203], s[100:101], 0, v[200:201]
	global_load_dword v204, v[202:203], off
	global_load_dword v205, v[202:203], off offset:2048
	v_readlane_b32 s100, v253, 35
	v_readlane_b32 s101, v253, 36
	s_add_u32 s100, s100, 0x7000
	s_addc_u32 s101, s101, 0
	v_lshl_add_u64 v[202:203], s[100:101], 0, v[200:201]
	global_load_dword v206, v[202:203], off
	global_load_dword v207, v[202:203], off offset:2048
	v_readlane_b32 s100, v253, 37
	v_readlane_b32 s101, v253, 38
	s_add_u32 s100, s100, 0x7000
	s_addc_u32 s101, s101, 0
	v_lshl_add_u64 v[202:203], s[100:101], 0, v[200:201]
	global_load_dword v208, v[202:203], off
	global_load_dword v209, v[202:203], off offset:2048
	s_waitcnt vmcnt(0)
	ds_write2st64_b32 v200, v204, v205 offset1:8
	ds_write2st64_b32 v200, v206, v207 offset0:16 offset1:24
	ds_write2st64_b32 v200, v208, v209 offset0:32 offset1:40
	v_mov_b64_e32 v[0:1], s[24:25]
	v_pk_mul_f32 v[68:69], s[30:31], v[0:1] op_sel_hi:[1,0]
	v_pk_mul_f32 v[58:59], s[28:29], v[0:1] op_sel_hi:[1,0]
	s_waitcnt lgkmcnt(0)
	s_barrier
	ds_read_b128 v[0:3], v86
	ds_read_b128 v[4:7], v86 offset:1024
	ds_read_b128 v[8:11], v86 offset:2048
	ds_read_b128 v[12:15], v86 offset:3072
	ds_read_b128 v[16:19], v86 offset:4096
	ds_read_b128 v[20:23], v86 offset:5120
	ds_read_b128 v[24:27], v86 offset:8192
	ds_read_b128 v[28:31], v86 offset:9216
	ds_read_b128 v[32:35], v86 offset:6144
	ds_read_b128 v[36:39], v86 offset:7168
	ds_read_b128 v[40:43], v86 offset:10240
	ds_read_b128 v[44:47], v86 offset:11264
	s_add_i32 s10, s10, 32
	s_ashr_i32 s11, s10, 31
	s_lshl_b64 s[10:11], s[10:11], 11
	s_or_b32 s33, s33, 3
	v_lshl_add_u64 v[56:57], v[50:51], 0, s[10:11]
	s_mov_b32 s35, 0
	s_mov_b64 s[10:11], -1
	s_mov_b64 s[30:31], 0
	s_branch .LBB0_3810
